# plus pipelined score-row loads: the four 32-key groups overlap (next group's loads issued before the current group's selects); radix-level broadcasts via v_readlane
# baseline (speedup 1.0000x reference)
; __device__ __forceinline__ void dsa2_unit(LAS unsigned char* lds, const bf16* PROJ, const bf16* KIDX, const bf16* KVN, bf16* OLAT, float* sbuf, int b, int t0, int tid) {
;     ...
;         const int n = t + 1, nreg = (n + 63) >> 6; const float* sr = sbuf + (size_t)wave * 8192;
;         unsigned kk[128];
;     ...
;         for (int repk = 0; repk < DUP_KK; ++repk)
; #pragma unroll
;         for (int gI = 0; gI < 4; ++gI) {
;             if (gI * 32 < nreg) {
;                 float fv[32];
; #pragma unroll
;                 for (int i = 0; i < 32; ++i) { const int key = lane + 64 * (gI * 32 + i); fv[i] = __hip_atomic_load(sr + (key < n ? key : n - 1), __ATOMIC_RELAXED, __HIP_MEMORY_SCOPE_AGENT); }
; #pragma unroll
;                 for (int i = 0; i < 32; ++i) { const int key = lane + 64 * (gI * 32 + i); kk[gI * 32 + i] = key < n ? __builtin_bit_cast(unsigned, fv[i]) : 0u; }
;             } else {
; #pragma unroll
;                 for (int i = 0; i < 32; ++i) kk[gI * 32 + i] = 0u;
;             }
;         }
.LBB0_720:
	s_add_i32 s1, s58, 64
	s_ashr_i32 s49, s1, 6
	s_ashr_i32 s1, s0, 31
	s_waitcnt vmcnt(0)
	s_lshl_b64 s[0:1], s[0:1], 15
	s_cmp_gt_i32 s49, 0
	s_cselect_b64 s[8:9], -1, 0
	s_cmp_lt_i32 s49, 1
	s_waitcnt vmcnt(0)
	v_lshl_add_u64 v[0:1], v[140:141], 0, s[0:1]
	s_barrier
	s_cbranch_scc1 .LBB0_722
	s_cmp_gt_i32 s49, 32
	s_cselect_b64 s[6:7], -1, 0
	s_cmp_gt_i32 s49, 64
	s_cselect_b64 s[18:19], -1, 0
	s_cmpk_gt_i32 s49, 0x60
	s_cselect_b64 s[16:17], -1, 0
	v_readfirstlane_b32 s2, v0
	v_readfirstlane_b32 s3, v1
	v_lshlrev_b32_e32 v2, 2, v129
	v_mov_b32_e32 v135, 0
	v_mov_b32_e32 v133, 0
	v_mov_b32_e32 v131, 0
	v_mov_b32_e32 v127, 0
	v_mov_b32_e32 v125, 0
	v_mov_b32_e32 v124, 0
	v_mov_b32_e32 v123, 0
	v_mov_b32_e32 v122, 0
	v_mov_b32_e32 v121, 0
	v_mov_b32_e32 v120, 0
	v_mov_b32_e32 v119, 0
	v_mov_b32_e32 v118, 0
	v_mov_b32_e32 v117, 0
	v_mov_b32_e32 v116, 0
	v_mov_b32_e32 v115, 0
	v_mov_b32_e32 v114, 0
	v_mov_b32_e32 v113, 0
	v_mov_b32_e32 v112, 0
	v_mov_b32_e32 v111, 0
	v_mov_b32_e32 v110, 0
	v_mov_b32_e32 v109, 0
	v_mov_b32_e32 v108, 0
	v_mov_b32_e32 v107, 0
	v_mov_b32_e32 v106, 0
	v_mov_b32_e32 v105, 0
	v_mov_b32_e32 v104, 0
	v_mov_b32_e32 v103, 0
	v_mov_b32_e32 v102, 0
	v_mov_b32_e32 v100, 0
	v_mov_b32_e32 v98, 0
	v_mov_b32_e32 v96, 0
	v_mov_b32_e32 v94, 0
	v_mov_b32_e32 v101, 0
	v_mov_b32_e32 v99, 0
	v_mov_b32_e32 v97, 0
	v_mov_b32_e32 v95, 0
	v_mov_b32_e32 v93, 0
	v_mov_b32_e32 v92, 0
	v_mov_b32_e32 v91, 0
	v_mov_b32_e32 v90, 0
	v_mov_b32_e32 v89, 0
	v_mov_b32_e32 v88, 0
	v_mov_b32_e32 v87, 0
	v_mov_b32_e32 v86, 0
	v_mov_b32_e32 v85, 0
	v_mov_b32_e32 v84, 0
	v_mov_b32_e32 v83, 0
	v_mov_b32_e32 v82, 0
	v_mov_b32_e32 v81, 0
	v_mov_b32_e32 v80, 0
	v_mov_b32_e32 v79, 0
	v_mov_b32_e32 v78, 0
	v_mov_b32_e32 v77, 0
	v_mov_b32_e32 v76, 0
	v_mov_b32_e32 v75, 0
	v_mov_b32_e32 v74, 0
	v_mov_b32_e32 v73, 0
	v_mov_b32_e32 v72, 0
	v_mov_b32_e32 v71, 0
	v_mov_b32_e32 v70, 0
	v_mov_b32_e32 v68, 0
	v_mov_b32_e32 v66, 0
	v_mov_b32_e32 v64, 0
	v_mov_b32_e32 v57, 0
	v_mov_b32_e32 v69, 0
	v_mov_b32_e32 v67, 0
	v_mov_b32_e32 v65, 0
	v_mov_b32_e32 v63, 0
	v_mov_b32_e32 v62, 0
	v_mov_b32_e32 v61, 0
	v_mov_b32_e32 v60, 0
	v_mov_b32_e32 v59, 0
	v_mov_b32_e32 v58, 0
	v_mov_b32_e32 v56, 0
	v_mov_b32_e32 v55, 0
	v_mov_b32_e32 v54, 0
	v_mov_b32_e32 v53, 0
	v_mov_b32_e32 v52, 0
	v_mov_b32_e32 v51, 0
	v_mov_b32_e32 v50, 0
	v_mov_b32_e32 v49, 0
	v_mov_b32_e32 v48, 0
	v_mov_b32_e32 v47, 0
	v_mov_b32_e32 v46, 0
	v_mov_b32_e32 v45, 0
	v_mov_b32_e32 v44, 0
	v_mov_b32_e32 v43, 0
	v_mov_b32_e32 v42, 0
	v_mov_b32_e32 v41, 0
	v_mov_b32_e32 v40, 0
	v_mov_b32_e32 v39, 0
	v_mov_b32_e32 v38, 0
	v_mov_b32_e32 v37, 0
	v_mov_b32_e32 v36, 0
	v_mov_b32_e32 v35, 0
	v_mov_b32_e32 v32, 0
	s_nop 3
	global_load_dword v166, v2, s[2:3] sc1
	global_load_dword v165, v2, s[2:3] offset:256 sc1
	global_load_dword v164, v2, s[2:3] offset:512 sc1
	global_load_dword v163, v2, s[2:3] offset:768 sc1
	global_load_dword v162, v2, s[2:3] offset:1024 sc1
	global_load_dword v161, v2, s[2:3] offset:1280 sc1
	global_load_dword v160, v2, s[2:3] offset:1536 sc1
	global_load_dword v159, v2, s[2:3] offset:1792 sc1
	global_load_dword v158, v2, s[2:3] offset:2048 sc1
	global_load_dword v157, v2, s[2:3] offset:2304 sc1
	global_load_dword v155, v2, s[2:3] offset:2560 sc1
	global_load_dword v154, v2, s[2:3] offset:2816 sc1
	global_load_dword v153, v2, s[2:3] offset:3072 sc1
	global_load_dword v152, v2, s[2:3] offset:3328 sc1
	global_load_dword v151, v2, s[2:3] offset:3584 sc1
	global_load_dword v149, v2, s[2:3] offset:3840 sc1
	s_add_u32 s2, s2, 0x1000
	s_addc_u32 s3, s3, 0
	global_load_dword v148, v2, s[2:3] sc1
	global_load_dword v147, v2, s[2:3] offset:256 sc1
	global_load_dword v146, v2, s[2:3] offset:512 sc1
	global_load_dword v145, v2, s[2:3] offset:768 sc1
	global_load_dword v144, v2, s[2:3] offset:1024 sc1
	global_load_dword v143, v2, s[2:3] offset:1280 sc1
	global_load_dword v142, v2, s[2:3] offset:1536 sc1
	global_load_dword v141, v2, s[2:3] offset:1792 sc1
	global_load_dword v140, v2, s[2:3] offset:2048 sc1
	global_load_dword v139, v2, s[2:3] offset:2304 sc1
	global_load_dword v137, v2, s[2:3] offset:2560 sc1
	global_load_dword v136, v2, s[2:3] offset:2816 sc1
	global_load_dword v134, v2, s[2:3] offset:3072 sc1
	global_load_dword v132, v2, s[2:3] offset:3328 sc1
	global_load_dword v130, v2, s[2:3] offset:3584 sc1
	global_load_dword v126, v2, s[2:3] offset:3840 sc1
	s_cmp_gt_i32 s49, 32
	s_cbranch_scc0 .Lkk2_last0
; __device__ __forceinline__ void dsa2_unit(LAS unsigned char* lds, const bf16* PROJ, const bf16* KIDX, const bf16* KVN, bf16* OLAT, float* sbuf, int b, int t0, int tid) {
;     ...
;         for (int repk = 0; repk < DUP_KK; ++repk)
; #pragma unroll
;         for (int gI = 0; gI < 4; ++gI) {
;             if (gI * 32 < nreg) {
;                 float fv[32];
; #pragma unroll
;                 for (int i = 0; i < 32; ++i) { const int key = lane + 64 * (gI * 32 + i); fv[i] = __hip_atomic_load(sr + (key < n ? key : n - 1), __ATOMIC_RELAXED, __HIP_MEMORY_SCOPE_AGENT); }
; #pragma unroll
;                 for (int i = 0; i < 32; ++i) { const int key = lane + 64 * (gI * 32 + i); kk[gI * 32 + i] = key < n ? __builtin_bit_cast(unsigned, fv[i]) : 0u; }
	s_add_u32 s2, s2, 0x1000
	s_addc_u32 s3, s3, 0
	global_load_dword v135, v2, s[2:3] sc1
	global_load_dword v133, v2, s[2:3] offset:256 sc1
	global_load_dword v131, v2, s[2:3] offset:512 sc1
	global_load_dword v127, v2, s[2:3] offset:768 sc1
	global_load_dword v125, v2, s[2:3] offset:1024 sc1
	global_load_dword v124, v2, s[2:3] offset:1280 sc1
	global_load_dword v123, v2, s[2:3] offset:1536 sc1
	global_load_dword v122, v2, s[2:3] offset:1792 sc1
	global_load_dword v121, v2, s[2:3] offset:2048 sc1
	global_load_dword v120, v2, s[2:3] offset:2304 sc1
	global_load_dword v119, v2, s[2:3] offset:2560 sc1
	global_load_dword v118, v2, s[2:3] offset:2816 sc1
	global_load_dword v117, v2, s[2:3] offset:3072 sc1
	global_load_dword v116, v2, s[2:3] offset:3328 sc1
	global_load_dword v115, v2, s[2:3] offset:3584 sc1
	global_load_dword v114, v2, s[2:3] offset:3840 sc1
	s_add_u32 s2, s2, 0x1000
	s_addc_u32 s3, s3, 0
	global_load_dword v113, v2, s[2:3] sc1
	global_load_dword v112, v2, s[2:3] offset:256 sc1
	global_load_dword v111, v2, s[2:3] offset:512 sc1
	global_load_dword v110, v2, s[2:3] offset:768 sc1
	global_load_dword v109, v2, s[2:3] offset:1024 sc1
	global_load_dword v108, v2, s[2:3] offset:1280 sc1
	global_load_dword v107, v2, s[2:3] offset:1536 sc1
	global_load_dword v106, v2, s[2:3] offset:1792 sc1
	global_load_dword v105, v2, s[2:3] offset:2048 sc1
	global_load_dword v104, v2, s[2:3] offset:2304 sc1
	global_load_dword v103, v2, s[2:3] offset:2560 sc1
	global_load_dword v102, v2, s[2:3] offset:2816 sc1
	s_add_i32 s4, s58, 1
	v_cmp_gt_i32_e64 s[10:11], s4, v129
	s_sub_i32 s4, s4, 64
	v_cmp_gt_i32_e64 s[12:13], s4, v129
	s_sub_i32 s4, s4, 64
	v_cmp_gt_i32_e64 s[14:15], s4, v129
	s_sub_i32 s4, s4, 64
	v_cmp_gt_i32_e32 vcc, s4, v129
	s_sub_i32 s4, s4, 64
	s_waitcnt vmcnt(56)
	v_cndmask_b32_e64 v166, 0, v166, s[10:11]
	v_cndmask_b32_e64 v165, 0, v165, s[12:13]
	v_cndmask_b32_e64 v164, 0, v164, s[14:15]
	v_cndmask_b32_e32 v163, 0, v163, vcc
	global_load_dword v100, v2, s[2:3] offset:3072 sc1
	global_load_dword v98, v2, s[2:3] offset:3328 sc1
	global_load_dword v96, v2, s[2:3] offset:3584 sc1
	global_load_dword v94, v2, s[2:3] offset:3840 sc1
	v_cmp_gt_i32_e64 s[10:11], s4, v129
	s_sub_i32 s4, s4, 64
	v_cmp_gt_i32_e64 s[12:13], s4, v129
	s_sub_i32 s4, s4, 64
	v_cmp_gt_i32_e64 s[14:15], s4, v129
	s_sub_i32 s4, s4, 64
	v_cmp_gt_i32_e32 vcc, s4, v129
	s_sub_i32 s4, s4, 64
	s_waitcnt vmcnt(56)
	v_cndmask_b32_e64 v162, 0, v162, s[10:11]
	v_cndmask_b32_e64 v161, 0, v161, s[12:13]
	v_cndmask_b32_e64 v160, 0, v160, s[14:15]
	v_cndmask_b32_e32 v159, 0, v159, vcc
	v_cmp_gt_i32_e64 s[10:11], s4, v129
	s_sub_i32 s4, s4, 64
	v_cmp_gt_i32_e64 s[12:13], s4, v129
	s_sub_i32 s4, s4, 64
	v_cmp_gt_i32_e64 s[14:15], s4, v129
	s_sub_i32 s4, s4, 64
	v_cmp_gt_i32_e32 vcc, s4, v129
	s_sub_i32 s4, s4, 64
	s_waitcnt vmcnt(52)
	v_cndmask_b32_e64 v158, 0, v158, s[10:11]
	v_cndmask_b32_e64 v157, 0, v157, s[12:13]
	v_cndmask_b32_e64 v155, 0, v155, s[14:15]
	v_cndmask_b32_e32 v154, 0, v154, vcc
	v_cmp_gt_i32_e64 s[10:11], s4, v129
	s_sub_i32 s4, s4, 64
	v_cmp_gt_i32_e64 s[12:13], s4, v129
	s_sub_i32 s4, s4, 64
	v_cmp_gt_i32_e64 s[14:15], s4, v129
	s_sub_i32 s4, s4, 64
	v_cmp_gt_i32_e32 vcc, s4, v129
	s_sub_i32 s4, s4, 64
	s_waitcnt vmcnt(48)
	v_cndmask_b32_e64 v153, 0, v153, s[10:11]
	v_cndmask_b32_e64 v152, 0, v152, s[12:13]
	v_cndmask_b32_e64 v151, 0, v151, s[14:15]
	v_cndmask_b32_e32 v149, 0, v149, vcc
	v_cmp_gt_i32_e64 s[10:11], s4, v129
	s_sub_i32 s4, s4, 64
	v_cmp_gt_i32_e64 s[12:13], s4, v129
	s_sub_i32 s4, s4, 64
	v_cmp_gt_i32_e64 s[14:15], s4, v129
	s_sub_i32 s4, s4, 64
	v_cmp_gt_i32_e32 vcc, s4, v129
	s_sub_i32 s4, s4, 64
	s_waitcnt vmcnt(44)
	v_cndmask_b32_e64 v148, 0, v148, s[10:11]
	v_cndmask_b32_e64 v147, 0, v147, s[12:13]
	v_cndmask_b32_e64 v146, 0, v146, s[14:15]
	v_cndmask_b32_e32 v145, 0, v145, vcc
	v_cmp_gt_i32_e64 s[10:11], s4, v129
	s_sub_i32 s4, s4, 64
	v_cmp_gt_i32_e64 s[12:13], s4, v129
	s_sub_i32 s4, s4, 64
	v_cmp_gt_i32_e64 s[14:15], s4, v129
	s_sub_i32 s4, s4, 64
	v_cmp_gt_i32_e32 vcc, s4, v129
	s_sub_i32 s4, s4, 64
	s_waitcnt vmcnt(40)
	v_cndmask_b32_e64 v144, 0, v144, s[10:11]
	v_cndmask_b32_e64 v143, 0, v143, s[12:13]
	v_cndmask_b32_e64 v142, 0, v142, s[14:15]
	v_cndmask_b32_e32 v141, 0, v141, vcc
	v_cmp_gt_i32_e64 s[10:11], s4, v129
	s_sub_i32 s4, s4, 64
	v_cmp_gt_i32_e64 s[12:13], s4, v129
	s_sub_i32 s4, s4, 64
	v_cmp_gt_i32_e64 s[14:15], s4, v129
	s_sub_i32 s4, s4, 64
	v_cmp_gt_i32_e32 vcc, s4, v129
	s_sub_i32 s4, s4, 64
	s_waitcnt vmcnt(36)
	v_cndmask_b32_e64 v140, 0, v140, s[10:11]
	v_cndmask_b32_e64 v139, 0, v139, s[12:13]
	v_cndmask_b32_e64 v137, 0, v137, s[14:15]
	v_cndmask_b32_e32 v136, 0, v136, vcc
	v_cmp_gt_i32_e64 s[10:11], s4, v129
	s_sub_i32 s4, s4, 64
	v_cmp_gt_i32_e64 s[12:13], s4, v129
	s_sub_i32 s4, s4, 64
	v_cmp_gt_i32_e64 s[14:15], s4, v129
	s_sub_i32 s4, s4, 64
	v_cmp_gt_i32_e32 vcc, s4, v129
	s_sub_i32 s4, s4, 64
	s_waitcnt vmcnt(32)
	v_cndmask_b32_e64 v134, 0, v134, s[10:11]
	v_cndmask_b32_e64 v132, 0, v132, s[12:13]
	v_cndmask_b32_e64 v130, 0, v130, s[14:15]
	v_cndmask_b32_e32 v126, 0, v126, vcc
	s_cmp_gt_i32 s49, 64
	s_cbranch_scc0 .Lkk2_last1
; __device__ __forceinline__ void dsa2_unit(LAS unsigned char* lds, const bf16* PROJ, const bf16* KIDX, const bf16* KVN, bf16* OLAT, float* sbuf, int b, int t0, int tid) {
;     ...
;         for (int repk = 0; repk < DUP_KK; ++repk)
; #pragma unroll
;         for (int gI = 0; gI < 4; ++gI) {
;             if (gI * 32 < nreg) {
;                 float fv[32];
; #pragma unroll
;                 for (int i = 0; i < 32; ++i) { const int key = lane + 64 * (gI * 32 + i); fv[i] = __hip_atomic_load(sr + (key < n ? key : n - 1), __ATOMIC_RELAXED, __HIP_MEMORY_SCOPE_AGENT); }
; #pragma unroll
;                 for (int i = 0; i < 32; ++i) { const int key = lane + 64 * (gI * 32 + i); kk[gI * 32 + i] = key < n ? __builtin_bit_cast(unsigned, fv[i]) : 0u; }
	s_add_u32 s2, s2, 0x1000
	s_addc_u32 s3, s3, 0
	global_load_dword v101, v2, s[2:3] sc1
	global_load_dword v99, v2, s[2:3] offset:256 sc1
	global_load_dword v97, v2, s[2:3] offset:512 sc1
	global_load_dword v95, v2, s[2:3] offset:768 sc1
	global_load_dword v93, v2, s[2:3] offset:1024 sc1
	global_load_dword v92, v2, s[2:3] offset:1280 sc1
	global_load_dword v91, v2, s[2:3] offset:1536 sc1
	global_load_dword v90, v2, s[2:3] offset:1792 sc1
	global_load_dword v89, v2, s[2:3] offset:2048 sc1
	global_load_dword v88, v2, s[2:3] offset:2304 sc1
	global_load_dword v87, v2, s[2:3] offset:2560 sc1
	global_load_dword v86, v2, s[2:3] offset:2816 sc1
	global_load_dword v85, v2, s[2:3] offset:3072 sc1
	global_load_dword v84, v2, s[2:3] offset:3328 sc1
	global_load_dword v83, v2, s[2:3] offset:3584 sc1
	global_load_dword v82, v2, s[2:3] offset:3840 sc1
	s_add_u32 s2, s2, 0x1000
	s_addc_u32 s3, s3, 0
	global_load_dword v81, v2, s[2:3] sc1
	global_load_dword v80, v2, s[2:3] offset:256 sc1
	global_load_dword v79, v2, s[2:3] offset:512 sc1
	global_load_dword v78, v2, s[2:3] offset:768 sc1
	global_load_dword v77, v2, s[2:3] offset:1024 sc1
	global_load_dword v76, v2, s[2:3] offset:1280 sc1
	global_load_dword v75, v2, s[2:3] offset:1536 sc1
	global_load_dword v74, v2, s[2:3] offset:1792 sc1
	global_load_dword v73, v2, s[2:3] offset:2048 sc1
	global_load_dword v72, v2, s[2:3] offset:2304 sc1
	global_load_dword v71, v2, s[2:3] offset:2560 sc1
	global_load_dword v70, v2, s[2:3] offset:2816 sc1
	s_add_i32 s4, s58, -2047
	v_cmp_gt_i32_e64 s[10:11], s4, v129
	s_sub_i32 s4, s4, 64
	v_cmp_gt_i32_e64 s[12:13], s4, v129
	s_sub_i32 s4, s4, 64
	v_cmp_gt_i32_e64 s[14:15], s4, v129
	s_sub_i32 s4, s4, 64
	v_cmp_gt_i32_e32 vcc, s4, v129
	s_sub_i32 s4, s4, 64
	s_waitcnt vmcnt(56)
	v_cndmask_b32_e64 v135, 0, v135, s[10:11]
	v_cndmask_b32_e64 v133, 0, v133, s[12:13]
	v_cndmask_b32_e64 v131, 0, v131, s[14:15]
	v_cndmask_b32_e32 v127, 0, v127, vcc
	global_load_dword v68, v2, s[2:3] offset:3072 sc1
	global_load_dword v66, v2, s[2:3] offset:3328 sc1
	global_load_dword v64, v2, s[2:3] offset:3584 sc1
	global_load_dword v57, v2, s[2:3] offset:3840 sc1
	v_cmp_gt_i32_e64 s[10:11], s4, v129
	s_sub_i32 s4, s4, 64
	v_cmp_gt_i32_e64 s[12:13], s4, v129
	s_sub_i32 s4, s4, 64
	v_cmp_gt_i32_e64 s[14:15], s4, v129
	s_sub_i32 s4, s4, 64
	v_cmp_gt_i32_e32 vcc, s4, v129
	s_sub_i32 s4, s4, 64
	s_waitcnt vmcnt(56)
	v_cndmask_b32_e64 v125, 0, v125, s[10:11]
	v_cndmask_b32_e64 v124, 0, v124, s[12:13]
	v_cndmask_b32_e64 v123, 0, v123, s[14:15]
	v_cndmask_b32_e32 v122, 0, v122, vcc
	v_cmp_gt_i32_e64 s[10:11], s4, v129
	s_sub_i32 s4, s4, 64
	v_cmp_gt_i32_e64 s[12:13], s4, v129
	s_sub_i32 s4, s4, 64
	v_cmp_gt_i32_e64 s[14:15], s4, v129
	s_sub_i32 s4, s4, 64
	v_cmp_gt_i32_e32 vcc, s4, v129
	s_sub_i32 s4, s4, 64
	s_waitcnt vmcnt(52)
	v_cndmask_b32_e64 v121, 0, v121, s[10:11]
	v_cndmask_b32_e64 v120, 0, v120, s[12:13]
	v_cndmask_b32_e64 v119, 0, v119, s[14:15]
	v_cndmask_b32_e32 v118, 0, v118, vcc
	v_cmp_gt_i32_e64 s[10:11], s4, v129
	s_sub_i32 s4, s4, 64
	v_cmp_gt_i32_e64 s[12:13], s4, v129
	s_sub_i32 s4, s4, 64
	v_cmp_gt_i32_e64 s[14:15], s4, v129
	s_sub_i32 s4, s4, 64
	v_cmp_gt_i32_e32 vcc, s4, v129
	s_sub_i32 s4, s4, 64
	s_waitcnt vmcnt(48)
	v_cndmask_b32_e64 v117, 0, v117, s[10:11]
	v_cndmask_b32_e64 v116, 0, v116, s[12:13]
	v_cndmask_b32_e64 v115, 0, v115, s[14:15]
	v_cndmask_b32_e32 v114, 0, v114, vcc
	v_cmp_gt_i32_e64 s[10:11], s4, v129
	s_sub_i32 s4, s4, 64
	v_cmp_gt_i32_e64 s[12:13], s4, v129
	s_sub_i32 s4, s4, 64
	v_cmp_gt_i32_e64 s[14:15], s4, v129
	s_sub_i32 s4, s4, 64
	v_cmp_gt_i32_e32 vcc, s4, v129
	s_sub_i32 s4, s4, 64
	s_waitcnt vmcnt(44)
	v_cndmask_b32_e64 v113, 0, v113, s[10:11]
	v_cndmask_b32_e64 v112, 0, v112, s[12:13]
	v_cndmask_b32_e64 v111, 0, v111, s[14:15]
	v_cndmask_b32_e32 v110, 0, v110, vcc
	v_cmp_gt_i32_e64 s[10:11], s4, v129
	s_sub_i32 s4, s4, 64
	v_cmp_gt_i32_e64 s[12:13], s4, v129
	s_sub_i32 s4, s4, 64
	v_cmp_gt_i32_e64 s[14:15], s4, v129
	s_sub_i32 s4, s4, 64
	v_cmp_gt_i32_e32 vcc, s4, v129
	s_sub_i32 s4, s4, 64
	s_waitcnt vmcnt(40)
	v_cndmask_b32_e64 v109, 0, v109, s[10:11]
	v_cndmask_b32_e64 v108, 0, v108, s[12:13]
	v_cndmask_b32_e64 v107, 0, v107, s[14:15]
	v_cndmask_b32_e32 v106, 0, v106, vcc
	v_cmp_gt_i32_e64 s[10:11], s4, v129
	s_sub_i32 s4, s4, 64
	v_cmp_gt_i32_e64 s[12:13], s4, v129
	s_sub_i32 s4, s4, 64
	v_cmp_gt_i32_e64 s[14:15], s4, v129
	s_sub_i32 s4, s4, 64
	v_cmp_gt_i32_e32 vcc, s4, v129
	s_sub_i32 s4, s4, 64
	s_waitcnt vmcnt(36)
	v_cndmask_b32_e64 v105, 0, v105, s[10:11]
	v_cndmask_b32_e64 v104, 0, v104, s[12:13]
	v_cndmask_b32_e64 v103, 0, v103, s[14:15]
	v_cndmask_b32_e32 v102, 0, v102, vcc
	v_cmp_gt_i32_e64 s[10:11], s4, v129
	s_sub_i32 s4, s4, 64
	v_cmp_gt_i32_e64 s[12:13], s4, v129
	s_sub_i32 s4, s4, 64
	v_cmp_gt_i32_e64 s[14:15], s4, v129
	s_sub_i32 s4, s4, 64
	v_cmp_gt_i32_e32 vcc, s4, v129
	s_sub_i32 s4, s4, 64
	s_waitcnt vmcnt(32)
	v_cndmask_b32_e64 v100, 0, v100, s[10:11]
	v_cndmask_b32_e64 v98, 0, v98, s[12:13]
	v_cndmask_b32_e64 v96, 0, v96, s[14:15]
	v_cndmask_b32_e32 v94, 0, v94, vcc
	s_cmp_gt_i32 s49, 96
	s_cbranch_scc0 .Lkk2_last2
; __device__ __forceinline__ void dsa2_unit(LAS unsigned char* lds, const bf16* PROJ, const bf16* KIDX, const bf16* KVN, bf16* OLAT, float* sbuf, int b, int t0, int tid) {
;     ...
;         for (int gI = 0; gI < 4; ++gI) {
;             if (gI * 32 < nreg) {
;                 float fv[32];
; #pragma unroll
;                 for (int i = 0; i < 32; ++i) { const int key = lane + 64 * (gI * 32 + i); fv[i] = __hip_atomic_load(sr + (key < n ? key : n - 1), __ATOMIC_RELAXED, __HIP_MEMORY_SCOPE_AGENT); }
; #pragma unroll
;                 for (int i = 0; i < 32; ++i) { const int key = lane + 64 * (gI * 32 + i); kk[gI * 32 + i] = key < n ? __builtin_bit_cast(unsigned, fv[i]) : 0u; }
;             } else {
; #pragma unroll
;                 for (int i = 0; i < 32; ++i) kk[gI * 32 + i] = 0u;
;             }
;         }
	s_add_u32 s2, s2, 0x1000
	s_addc_u32 s3, s3, 0
	global_load_dword v69, v2, s[2:3] sc1
	global_load_dword v67, v2, s[2:3] offset:256 sc1
	global_load_dword v65, v2, s[2:3] offset:512 sc1
	global_load_dword v63, v2, s[2:3] offset:768 sc1
	global_load_dword v62, v2, s[2:3] offset:1024 sc1
	global_load_dword v61, v2, s[2:3] offset:1280 sc1
	global_load_dword v60, v2, s[2:3] offset:1536 sc1
	global_load_dword v59, v2, s[2:3] offset:1792 sc1
	global_load_dword v58, v2, s[2:3] offset:2048 sc1
	global_load_dword v56, v2, s[2:3] offset:2304 sc1
	global_load_dword v55, v2, s[2:3] offset:2560 sc1
	global_load_dword v54, v2, s[2:3] offset:2816 sc1
	global_load_dword v53, v2, s[2:3] offset:3072 sc1
	global_load_dword v52, v2, s[2:3] offset:3328 sc1
	global_load_dword v51, v2, s[2:3] offset:3584 sc1
	global_load_dword v50, v2, s[2:3] offset:3840 sc1
	s_add_u32 s2, s2, 0x1000
	s_addc_u32 s3, s3, 0
	global_load_dword v49, v2, s[2:3] sc1
	global_load_dword v48, v2, s[2:3] offset:256 sc1
	global_load_dword v47, v2, s[2:3] offset:512 sc1
	global_load_dword v46, v2, s[2:3] offset:768 sc1
	global_load_dword v45, v2, s[2:3] offset:1024 sc1
	global_load_dword v44, v2, s[2:3] offset:1280 sc1
	global_load_dword v43, v2, s[2:3] offset:1536 sc1
	global_load_dword v42, v2, s[2:3] offset:1792 sc1
	global_load_dword v41, v2, s[2:3] offset:2048 sc1
	global_load_dword v40, v2, s[2:3] offset:2304 sc1
	global_load_dword v39, v2, s[2:3] offset:2560 sc1
	global_load_dword v38, v2, s[2:3] offset:2816 sc1
	s_add_i32 s4, s58, -4095
	v_cmp_gt_i32_e64 s[10:11], s4, v129
	s_sub_i32 s4, s4, 64
	v_cmp_gt_i32_e64 s[12:13], s4, v129
	s_sub_i32 s4, s4, 64
	v_cmp_gt_i32_e64 s[14:15], s4, v129
	s_sub_i32 s4, s4, 64
	v_cmp_gt_i32_e32 vcc, s4, v129
	s_sub_i32 s4, s4, 64
	s_waitcnt vmcnt(56)
	v_cndmask_b32_e64 v101, 0, v101, s[10:11]
	v_cndmask_b32_e64 v99, 0, v99, s[12:13]
	v_cndmask_b32_e64 v97, 0, v97, s[14:15]
	v_cndmask_b32_e32 v95, 0, v95, vcc
	global_load_dword v37, v2, s[2:3] offset:3072 sc1
	global_load_dword v36, v2, s[2:3] offset:3328 sc1
	global_load_dword v35, v2, s[2:3] offset:3584 sc1
	global_load_dword v32, v2, s[2:3] offset:3840 sc1
	v_cmp_gt_i32_e64 s[10:11], s4, v129
	s_sub_i32 s4, s4, 64
	v_cmp_gt_i32_e64 s[12:13], s4, v129
	s_sub_i32 s4, s4, 64
	v_cmp_gt_i32_e64 s[14:15], s4, v129
	s_sub_i32 s4, s4, 64
	v_cmp_gt_i32_e32 vcc, s4, v129
	s_sub_i32 s4, s4, 64
	s_waitcnt vmcnt(56)
	v_cndmask_b32_e64 v93, 0, v93, s[10:11]
	v_cndmask_b32_e64 v92, 0, v92, s[12:13]
	v_cndmask_b32_e64 v91, 0, v91, s[14:15]
	v_cndmask_b32_e32 v90, 0, v90, vcc
	v_cmp_gt_i32_e64 s[10:11], s4, v129
	s_sub_i32 s4, s4, 64
	v_cmp_gt_i32_e64 s[12:13], s4, v129
	s_sub_i32 s4, s4, 64
	v_cmp_gt_i32_e64 s[14:15], s4, v129
	s_sub_i32 s4, s4, 64
	v_cmp_gt_i32_e32 vcc, s4, v129
	s_sub_i32 s4, s4, 64
	s_waitcnt vmcnt(52)
	v_cndmask_b32_e64 v89, 0, v89, s[10:11]
	v_cndmask_b32_e64 v88, 0, v88, s[12:13]
	v_cndmask_b32_e64 v87, 0, v87, s[14:15]
	v_cndmask_b32_e32 v86, 0, v86, vcc
	v_cmp_gt_i32_e64 s[10:11], s4, v129
	s_sub_i32 s4, s4, 64
	v_cmp_gt_i32_e64 s[12:13], s4, v129
	s_sub_i32 s4, s4, 64
	v_cmp_gt_i32_e64 s[14:15], s4, v129
	s_sub_i32 s4, s4, 64
	v_cmp_gt_i32_e32 vcc, s4, v129
	s_sub_i32 s4, s4, 64
	s_waitcnt vmcnt(48)
	v_cndmask_b32_e64 v85, 0, v85, s[10:11]
	v_cndmask_b32_e64 v84, 0, v84, s[12:13]
	v_cndmask_b32_e64 v83, 0, v83, s[14:15]
	v_cndmask_b32_e32 v82, 0, v82, vcc
	v_cmp_gt_i32_e64 s[10:11], s4, v129
	s_sub_i32 s4, s4, 64
	v_cmp_gt_i32_e64 s[12:13], s4, v129
	s_sub_i32 s4, s4, 64
	v_cmp_gt_i32_e64 s[14:15], s4, v129
	s_sub_i32 s4, s4, 64
	v_cmp_gt_i32_e32 vcc, s4, v129
	s_sub_i32 s4, s4, 64
	s_waitcnt vmcnt(44)
	v_cndmask_b32_e64 v81, 0, v81, s[10:11]
	v_cndmask_b32_e64 v80, 0, v80, s[12:13]
	v_cndmask_b32_e64 v79, 0, v79, s[14:15]
	v_cndmask_b32_e32 v78, 0, v78, vcc
	v_cmp_gt_i32_e64 s[10:11], s4, v129
	s_sub_i32 s4, s4, 64
	v_cmp_gt_i32_e64 s[12:13], s4, v129
	s_sub_i32 s4, s4, 64
	v_cmp_gt_i32_e64 s[14:15], s4, v129
	s_sub_i32 s4, s4, 64
	v_cmp_gt_i32_e32 vcc, s4, v129
	s_sub_i32 s4, s4, 64
	s_waitcnt vmcnt(40)
	v_cndmask_b32_e64 v77, 0, v77, s[10:11]
	v_cndmask_b32_e64 v76, 0, v76, s[12:13]
	v_cndmask_b32_e64 v75, 0, v75, s[14:15]
	v_cndmask_b32_e32 v74, 0, v74, vcc
	v_cmp_gt_i32_e64 s[10:11], s4, v129
	s_sub_i32 s4, s4, 64
	v_cmp_gt_i32_e64 s[12:13], s4, v129
	s_sub_i32 s4, s4, 64
	v_cmp_gt_i32_e64 s[14:15], s4, v129
	s_sub_i32 s4, s4, 64
	v_cmp_gt_i32_e32 vcc, s4, v129
	s_sub_i32 s4, s4, 64
	s_waitcnt vmcnt(36)
	v_cndmask_b32_e64 v73, 0, v73, s[10:11]
	v_cndmask_b32_e64 v72, 0, v72, s[12:13]
	v_cndmask_b32_e64 v71, 0, v71, s[14:15]
	v_cndmask_b32_e32 v70, 0, v70, vcc
	v_cmp_gt_i32_e64 s[10:11], s4, v129
	s_sub_i32 s4, s4, 64
	v_cmp_gt_i32_e64 s[12:13], s4, v129
	s_sub_i32 s4, s4, 64
	v_cmp_gt_i32_e64 s[14:15], s4, v129
	s_sub_i32 s4, s4, 64
	v_cmp_gt_i32_e32 vcc, s4, v129
	s_sub_i32 s4, s4, 64
	s_waitcnt vmcnt(32)
	v_cndmask_b32_e64 v68, 0, v68, s[10:11]
	v_cndmask_b32_e64 v66, 0, v66, s[12:13]
	v_cndmask_b32_e64 v64, 0, v64, s[14:15]
	v_cndmask_b32_e32 v57, 0, v57, vcc
	s_add_i32 s4, s58, -6143
	v_cmp_gt_i32_e64 s[10:11], s4, v129
	s_sub_i32 s4, s4, 64
	v_cmp_gt_i32_e64 s[12:13], s4, v129
	s_sub_i32 s4, s4, 64
	v_cmp_gt_i32_e64 s[14:15], s4, v129
	s_sub_i32 s4, s4, 64
	v_cmp_gt_i32_e32 vcc, s4, v129
	s_sub_i32 s4, s4, 64
	s_waitcnt vmcnt(28)
	v_cndmask_b32_e64 v69, 0, v69, s[10:11]
	v_cndmask_b32_e64 v67, 0, v67, s[12:13]
	v_cndmask_b32_e64 v65, 0, v65, s[14:15]
	v_cndmask_b32_e32 v63, 0, v63, vcc
	v_cmp_gt_i32_e64 s[10:11], s4, v129
	s_sub_i32 s4, s4, 64
	v_cmp_gt_i32_e64 s[12:13], s4, v129
	s_sub_i32 s4, s4, 64
	v_cmp_gt_i32_e64 s[14:15], s4, v129
	s_sub_i32 s4, s4, 64
	v_cmp_gt_i32_e32 vcc, s4, v129
	s_sub_i32 s4, s4, 64
	s_waitcnt vmcnt(24)
; __device__ __forceinline__ void dsa2_unit(LAS unsigned char* lds, const bf16* PROJ, const bf16* KIDX, const bf16* KVN, bf16* OLAT, float* sbuf, int b, int t0, int tid) {
;     ...
;         for (int gI = 0; gI < 4; ++gI) {
;             if (gI * 32 < nreg) {
;                 float fv[32];
; #pragma unroll
;                 for (int i = 0; i < 32; ++i) { const int key = lane + 64 * (gI * 32 + i); fv[i] = __hip_atomic_load(sr + (key < n ? key : n - 1), __ATOMIC_RELAXED, __HIP_MEMORY_SCOPE_AGENT); }
; #pragma unroll
;                 for (int i = 0; i < 32; ++i) { const int key = lane + 64 * (gI * 32 + i); kk[gI * 32 + i] = key < n ? __builtin_bit_cast(unsigned, fv[i]) : 0u; }
;             } else {
; #pragma unroll
;                 for (int i = 0; i < 32; ++i) kk[gI * 32 + i] = 0u;
;             }
;         }
	v_cndmask_b32_e64 v62, 0, v62, s[10:11]
	v_cndmask_b32_e64 v61, 0, v61, s[12:13]
	v_cndmask_b32_e64 v60, 0, v60, s[14:15]
	v_cndmask_b32_e32 v59, 0, v59, vcc
	v_cmp_gt_i32_e64 s[10:11], s4, v129
	s_sub_i32 s4, s4, 64
	v_cmp_gt_i32_e64 s[12:13], s4, v129
	s_sub_i32 s4, s4, 64
	v_cmp_gt_i32_e64 s[14:15], s4, v129
	s_sub_i32 s4, s4, 64
	v_cmp_gt_i32_e32 vcc, s4, v129
	s_sub_i32 s4, s4, 64
	s_waitcnt vmcnt(20)
	v_cndmask_b32_e64 v58, 0, v58, s[10:11]
	v_cndmask_b32_e64 v56, 0, v56, s[12:13]
	v_cndmask_b32_e64 v55, 0, v55, s[14:15]
	v_cndmask_b32_e32 v54, 0, v54, vcc
	v_cmp_gt_i32_e64 s[10:11], s4, v129
	s_sub_i32 s4, s4, 64
	v_cmp_gt_i32_e64 s[12:13], s4, v129
	s_sub_i32 s4, s4, 64
	v_cmp_gt_i32_e64 s[14:15], s4, v129
	s_sub_i32 s4, s4, 64
	v_cmp_gt_i32_e32 vcc, s4, v129
	s_sub_i32 s4, s4, 64
	s_waitcnt vmcnt(16)
	v_cndmask_b32_e64 v53, 0, v53, s[10:11]
	v_cndmask_b32_e64 v52, 0, v52, s[12:13]
	v_cndmask_b32_e64 v51, 0, v51, s[14:15]
	v_cndmask_b32_e32 v50, 0, v50, vcc
	v_cmp_gt_i32_e64 s[10:11], s4, v129
	s_sub_i32 s4, s4, 64
	v_cmp_gt_i32_e64 s[12:13], s4, v129
	s_sub_i32 s4, s4, 64
	v_cmp_gt_i32_e64 s[14:15], s4, v129
	s_sub_i32 s4, s4, 64
	v_cmp_gt_i32_e32 vcc, s4, v129
	s_sub_i32 s4, s4, 64
	s_waitcnt vmcnt(12)
	v_cndmask_b32_e64 v49, 0, v49, s[10:11]
	v_cndmask_b32_e64 v48, 0, v48, s[12:13]
	v_cndmask_b32_e64 v47, 0, v47, s[14:15]
	v_cndmask_b32_e32 v46, 0, v46, vcc
	v_cmp_gt_i32_e64 s[10:11], s4, v129
	s_sub_i32 s4, s4, 64
	v_cmp_gt_i32_e64 s[12:13], s4, v129
	s_sub_i32 s4, s4, 64
	v_cmp_gt_i32_e64 s[14:15], s4, v129
	s_sub_i32 s4, s4, 64
	v_cmp_gt_i32_e32 vcc, s4, v129
	s_sub_i32 s4, s4, 64
	s_waitcnt vmcnt(8)
	v_cndmask_b32_e64 v45, 0, v45, s[10:11]
	v_cndmask_b32_e64 v44, 0, v44, s[12:13]
	v_cndmask_b32_e64 v43, 0, v43, s[14:15]
	v_cndmask_b32_e32 v42, 0, v42, vcc
	v_cmp_gt_i32_e64 s[10:11], s4, v129
	s_sub_i32 s4, s4, 64
	v_cmp_gt_i32_e64 s[12:13], s4, v129
	s_sub_i32 s4, s4, 64
	v_cmp_gt_i32_e64 s[14:15], s4, v129
	s_sub_i32 s4, s4, 64
	v_cmp_gt_i32_e32 vcc, s4, v129
	s_sub_i32 s4, s4, 64
	s_waitcnt vmcnt(4)
	v_cndmask_b32_e64 v41, 0, v41, s[10:11]
	v_cndmask_b32_e64 v40, 0, v40, s[12:13]
	v_cndmask_b32_e64 v39, 0, v39, s[14:15]
	v_cndmask_b32_e32 v38, 0, v38, vcc
	v_cmp_gt_i32_e64 s[10:11], s4, v129
	s_sub_i32 s4, s4, 64
	v_cmp_gt_i32_e64 s[12:13], s4, v129
	s_sub_i32 s4, s4, 64
	v_cmp_gt_i32_e64 s[14:15], s4, v129
	s_sub_i32 s4, s4, 64
	v_cmp_gt_i32_e32 vcc, s4, v129
	s_sub_i32 s4, s4, 64
	s_waitcnt vmcnt(0)
	v_cndmask_b32_e64 v37, 0, v37, s[10:11]
	v_cndmask_b32_e64 v36, 0, v36, s[12:13]
	v_cndmask_b32_e64 v35, 0, v35, s[14:15]
	v_cndmask_b32_e32 v32, 0, v32, vcc
	s_branch .LBB0_729
.Lkk2_last0:
	s_add_i32 s4, s58, 1
	v_cmp_gt_i32_e64 s[10:11], s4, v129
	s_sub_i32 s4, s4, 64
	v_cmp_gt_i32_e64 s[12:13], s4, v129
	s_sub_i32 s4, s4, 64
	v_cmp_gt_i32_e64 s[14:15], s4, v129
	s_sub_i32 s4, s4, 64
	v_cmp_gt_i32_e32 vcc, s4, v129
	s_sub_i32 s4, s4, 64
	s_waitcnt vmcnt(28)
	v_cndmask_b32_e64 v166, 0, v166, s[10:11]
	v_cndmask_b32_e64 v165, 0, v165, s[12:13]
	v_cndmask_b32_e64 v164, 0, v164, s[14:15]
	v_cndmask_b32_e32 v163, 0, v163, vcc
	v_cmp_gt_i32_e64 s[10:11], s4, v129
	s_sub_i32 s4, s4, 64
	v_cmp_gt_i32_e64 s[12:13], s4, v129
	s_sub_i32 s4, s4, 64
	v_cmp_gt_i32_e64 s[14:15], s4, v129
	s_sub_i32 s4, s4, 64
	v_cmp_gt_i32_e32 vcc, s4, v129
	s_sub_i32 s4, s4, 64
	s_waitcnt vmcnt(24)
	v_cndmask_b32_e64 v162, 0, v162, s[10:11]
	v_cndmask_b32_e64 v161, 0, v161, s[12:13]
	v_cndmask_b32_e64 v160, 0, v160, s[14:15]
	v_cndmask_b32_e32 v159, 0, v159, vcc
	v_cmp_gt_i32_e64 s[10:11], s4, v129
	s_sub_i32 s4, s4, 64
	v_cmp_gt_i32_e64 s[12:13], s4, v129
	s_sub_i32 s4, s4, 64
	v_cmp_gt_i32_e64 s[14:15], s4, v129
	s_sub_i32 s4, s4, 64
	v_cmp_gt_i32_e32 vcc, s4, v129
	s_sub_i32 s4, s4, 64
	s_waitcnt vmcnt(20)
	v_cndmask_b32_e64 v158, 0, v158, s[10:11]
	v_cndmask_b32_e64 v157, 0, v157, s[12:13]
	v_cndmask_b32_e64 v155, 0, v155, s[14:15]
	v_cndmask_b32_e32 v154, 0, v154, vcc
	v_cmp_gt_i32_e64 s[10:11], s4, v129
	s_sub_i32 s4, s4, 64
	v_cmp_gt_i32_e64 s[12:13], s4, v129
	s_sub_i32 s4, s4, 64
	v_cmp_gt_i32_e64 s[14:15], s4, v129
	s_sub_i32 s4, s4, 64
	v_cmp_gt_i32_e32 vcc, s4, v129
	s_sub_i32 s4, s4, 64
	s_waitcnt vmcnt(16)
	v_cndmask_b32_e64 v153, 0, v153, s[10:11]
	v_cndmask_b32_e64 v152, 0, v152, s[12:13]
	v_cndmask_b32_e64 v151, 0, v151, s[14:15]
	v_cndmask_b32_e32 v149, 0, v149, vcc
	v_cmp_gt_i32_e64 s[10:11], s4, v129
	s_sub_i32 s4, s4, 64
	v_cmp_gt_i32_e64 s[12:13], s4, v129
	s_sub_i32 s4, s4, 64
	v_cmp_gt_i32_e64 s[14:15], s4, v129
	s_sub_i32 s4, s4, 64
	v_cmp_gt_i32_e32 vcc, s4, v129
	s_sub_i32 s4, s4, 64
	s_waitcnt vmcnt(12)
	v_cndmask_b32_e64 v148, 0, v148, s[10:11]
	v_cndmask_b32_e64 v147, 0, v147, s[12:13]
	v_cndmask_b32_e64 v146, 0, v146, s[14:15]
	v_cndmask_b32_e32 v145, 0, v145, vcc
	v_cmp_gt_i32_e64 s[10:11], s4, v129
	s_sub_i32 s4, s4, 64
	v_cmp_gt_i32_e64 s[12:13], s4, v129
	s_sub_i32 s4, s4, 64
	v_cmp_gt_i32_e64 s[14:15], s4, v129
	s_sub_i32 s4, s4, 64
	v_cmp_gt_i32_e32 vcc, s4, v129
	s_sub_i32 s4, s4, 64
	s_waitcnt vmcnt(8)
	v_cndmask_b32_e64 v144, 0, v144, s[10:11]
	v_cndmask_b32_e64 v143, 0, v143, s[12:13]
	v_cndmask_b32_e64 v142, 0, v142, s[14:15]
	v_cndmask_b32_e32 v141, 0, v141, vcc
	v_cmp_gt_i32_e64 s[10:11], s4, v129
	s_sub_i32 s4, s4, 64
	v_cmp_gt_i32_e64 s[12:13], s4, v129
	s_sub_i32 s4, s4, 64
	v_cmp_gt_i32_e64 s[14:15], s4, v129
	s_sub_i32 s4, s4, 64
	v_cmp_gt_i32_e32 vcc, s4, v129
	s_sub_i32 s4, s4, 64
	s_waitcnt vmcnt(4)
	v_cndmask_b32_e64 v140, 0, v140, s[10:11]
	v_cndmask_b32_e64 v139, 0, v139, s[12:13]
	v_cndmask_b32_e64 v137, 0, v137, s[14:15]
	v_cndmask_b32_e32 v136, 0, v136, vcc
	v_cmp_gt_i32_e64 s[10:11], s4, v129
	s_sub_i32 s4, s4, 64
	v_cmp_gt_i32_e64 s[12:13], s4, v129
	s_sub_i32 s4, s4, 64
	v_cmp_gt_i32_e64 s[14:15], s4, v129
	s_sub_i32 s4, s4, 64
	v_cmp_gt_i32_e32 vcc, s4, v129
	s_sub_i32 s4, s4, 64
	s_waitcnt vmcnt(0)
	v_cndmask_b32_e64 v134, 0, v134, s[10:11]
	v_cndmask_b32_e64 v132, 0, v132, s[12:13]
	v_cndmask_b32_e64 v130, 0, v130, s[14:15]
	v_cndmask_b32_e32 v126, 0, v126, vcc
	s_branch .LBB0_729
; __device__ __forceinline__ void dsa2_unit(LAS unsigned char* lds, const bf16* PROJ, const bf16* KIDX, const bf16* KVN, bf16* OLAT, float* sbuf, int b, int t0, int tid) {
;     ...
;         for (int gI = 0; gI < 4; ++gI) {
;             if (gI * 32 < nreg) {
;                 float fv[32];
; #pragma unroll
;                 for (int i = 0; i < 32; ++i) { const int key = lane + 64 * (gI * 32 + i); fv[i] = __hip_atomic_load(sr + (key < n ? key : n - 1), __ATOMIC_RELAXED, __HIP_MEMORY_SCOPE_AGENT); }
; #pragma unroll
;                 for (int i = 0; i < 32; ++i) { const int key = lane + 64 * (gI * 32 + i); kk[gI * 32 + i] = key < n ? __builtin_bit_cast(unsigned, fv[i]) : 0u; }
;             } else {
; #pragma unroll
;                 for (int i = 0; i < 32; ++i) kk[gI * 32 + i] = 0u;
;             }
;         }
.Lkk2_last1:
	s_add_i32 s4, s58, -2047
	v_cmp_gt_i32_e64 s[10:11], s4, v129
	s_sub_i32 s4, s4, 64
	v_cmp_gt_i32_e64 s[12:13], s4, v129
	s_sub_i32 s4, s4, 64
	v_cmp_gt_i32_e64 s[14:15], s4, v129
	s_sub_i32 s4, s4, 64
	v_cmp_gt_i32_e32 vcc, s4, v129
	s_sub_i32 s4, s4, 64
	s_waitcnt vmcnt(28)
	v_cndmask_b32_e64 v135, 0, v135, s[10:11]
	v_cndmask_b32_e64 v133, 0, v133, s[12:13]
	v_cndmask_b32_e64 v131, 0, v131, s[14:15]
	v_cndmask_b32_e32 v127, 0, v127, vcc
	v_cmp_gt_i32_e64 s[10:11], s4, v129
	s_sub_i32 s4, s4, 64
	v_cmp_gt_i32_e64 s[12:13], s4, v129
	s_sub_i32 s4, s4, 64
	v_cmp_gt_i32_e64 s[14:15], s4, v129
	s_sub_i32 s4, s4, 64
	v_cmp_gt_i32_e32 vcc, s4, v129
	s_sub_i32 s4, s4, 64
	s_waitcnt vmcnt(24)
	v_cndmask_b32_e64 v125, 0, v125, s[10:11]
	v_cndmask_b32_e64 v124, 0, v124, s[12:13]
	v_cndmask_b32_e64 v123, 0, v123, s[14:15]
	v_cndmask_b32_e32 v122, 0, v122, vcc
	v_cmp_gt_i32_e64 s[10:11], s4, v129
	s_sub_i32 s4, s4, 64
	v_cmp_gt_i32_e64 s[12:13], s4, v129
	s_sub_i32 s4, s4, 64
	v_cmp_gt_i32_e64 s[14:15], s4, v129
	s_sub_i32 s4, s4, 64
	v_cmp_gt_i32_e32 vcc, s4, v129
	s_sub_i32 s4, s4, 64
	s_waitcnt vmcnt(20)
	v_cndmask_b32_e64 v121, 0, v121, s[10:11]
	v_cndmask_b32_e64 v120, 0, v120, s[12:13]
	v_cndmask_b32_e64 v119, 0, v119, s[14:15]
	v_cndmask_b32_e32 v118, 0, v118, vcc
	v_cmp_gt_i32_e64 s[10:11], s4, v129
	s_sub_i32 s4, s4, 64
	v_cmp_gt_i32_e64 s[12:13], s4, v129
	s_sub_i32 s4, s4, 64
	v_cmp_gt_i32_e64 s[14:15], s4, v129
	s_sub_i32 s4, s4, 64
	v_cmp_gt_i32_e32 vcc, s4, v129
	s_sub_i32 s4, s4, 64
	s_waitcnt vmcnt(16)
	v_cndmask_b32_e64 v117, 0, v117, s[10:11]
	v_cndmask_b32_e64 v116, 0, v116, s[12:13]
	v_cndmask_b32_e64 v115, 0, v115, s[14:15]
	v_cndmask_b32_e32 v114, 0, v114, vcc
	v_cmp_gt_i32_e64 s[10:11], s4, v129
	s_sub_i32 s4, s4, 64
	v_cmp_gt_i32_e64 s[12:13], s4, v129
	s_sub_i32 s4, s4, 64
	v_cmp_gt_i32_e64 s[14:15], s4, v129
	s_sub_i32 s4, s4, 64
	v_cmp_gt_i32_e32 vcc, s4, v129
	s_sub_i32 s4, s4, 64
	s_waitcnt vmcnt(12)
	v_cndmask_b32_e64 v113, 0, v113, s[10:11]
	v_cndmask_b32_e64 v112, 0, v112, s[12:13]
	v_cndmask_b32_e64 v111, 0, v111, s[14:15]
	v_cndmask_b32_e32 v110, 0, v110, vcc
	v_cmp_gt_i32_e64 s[10:11], s4, v129
	s_sub_i32 s4, s4, 64
	v_cmp_gt_i32_e64 s[12:13], s4, v129
	s_sub_i32 s4, s4, 64
	v_cmp_gt_i32_e64 s[14:15], s4, v129
	s_sub_i32 s4, s4, 64
	v_cmp_gt_i32_e32 vcc, s4, v129
	s_sub_i32 s4, s4, 64
	s_waitcnt vmcnt(8)
	v_cndmask_b32_e64 v109, 0, v109, s[10:11]
	v_cndmask_b32_e64 v108, 0, v108, s[12:13]
	v_cndmask_b32_e64 v107, 0, v107, s[14:15]
	v_cndmask_b32_e32 v106, 0, v106, vcc
	v_cmp_gt_i32_e64 s[10:11], s4, v129
	s_sub_i32 s4, s4, 64
	v_cmp_gt_i32_e64 s[12:13], s4, v129
	s_sub_i32 s4, s4, 64
	v_cmp_gt_i32_e64 s[14:15], s4, v129
	s_sub_i32 s4, s4, 64
	v_cmp_gt_i32_e32 vcc, s4, v129
	s_sub_i32 s4, s4, 64
	s_waitcnt vmcnt(4)
	v_cndmask_b32_e64 v105, 0, v105, s[10:11]
	v_cndmask_b32_e64 v104, 0, v104, s[12:13]
	v_cndmask_b32_e64 v103, 0, v103, s[14:15]
	v_cndmask_b32_e32 v102, 0, v102, vcc
	v_cmp_gt_i32_e64 s[10:11], s4, v129
	s_sub_i32 s4, s4, 64
	v_cmp_gt_i32_e64 s[12:13], s4, v129
	s_sub_i32 s4, s4, 64
	v_cmp_gt_i32_e64 s[14:15], s4, v129
	s_sub_i32 s4, s4, 64
	v_cmp_gt_i32_e32 vcc, s4, v129
	s_sub_i32 s4, s4, 64
	s_waitcnt vmcnt(0)
	v_cndmask_b32_e64 v100, 0, v100, s[10:11]
	v_cndmask_b32_e64 v98, 0, v98, s[12:13]
	v_cndmask_b32_e64 v96, 0, v96, s[14:15]
	v_cndmask_b32_e32 v94, 0, v94, vcc
	s_branch .LBB0_729
.Lkk2_last2:
	s_add_i32 s4, s58, -4095
	v_cmp_gt_i32_e64 s[10:11], s4, v129
	s_sub_i32 s4, s4, 64
	v_cmp_gt_i32_e64 s[12:13], s4, v129
	s_sub_i32 s4, s4, 64
	v_cmp_gt_i32_e64 s[14:15], s4, v129
	s_sub_i32 s4, s4, 64
	v_cmp_gt_i32_e32 vcc, s4, v129
	s_sub_i32 s4, s4, 64
	s_waitcnt vmcnt(28)
	v_cndmask_b32_e64 v101, 0, v101, s[10:11]
	v_cndmask_b32_e64 v99, 0, v99, s[12:13]
	v_cndmask_b32_e64 v97, 0, v97, s[14:15]
	v_cndmask_b32_e32 v95, 0, v95, vcc
	v_cmp_gt_i32_e64 s[10:11], s4, v129
	s_sub_i32 s4, s4, 64
	v_cmp_gt_i32_e64 s[12:13], s4, v129
	s_sub_i32 s4, s4, 64
	v_cmp_gt_i32_e64 s[14:15], s4, v129
	s_sub_i32 s4, s4, 64
	v_cmp_gt_i32_e32 vcc, s4, v129
	s_sub_i32 s4, s4, 64
	s_waitcnt vmcnt(24)
	v_cndmask_b32_e64 v93, 0, v93, s[10:11]
	v_cndmask_b32_e64 v92, 0, v92, s[12:13]
	v_cndmask_b32_e64 v91, 0, v91, s[14:15]
	v_cndmask_b32_e32 v90, 0, v90, vcc
	v_cmp_gt_i32_e64 s[10:11], s4, v129
	s_sub_i32 s4, s4, 64
	v_cmp_gt_i32_e64 s[12:13], s4, v129
	s_sub_i32 s4, s4, 64
	v_cmp_gt_i32_e64 s[14:15], s4, v129
	s_sub_i32 s4, s4, 64
	v_cmp_gt_i32_e32 vcc, s4, v129
	s_sub_i32 s4, s4, 64
	s_waitcnt vmcnt(20)
	v_cndmask_b32_e64 v89, 0, v89, s[10:11]
	v_cndmask_b32_e64 v88, 0, v88, s[12:13]
	v_cndmask_b32_e64 v87, 0, v87, s[14:15]
	v_cndmask_b32_e32 v86, 0, v86, vcc
	v_cmp_gt_i32_e64 s[10:11], s4, v129
	s_sub_i32 s4, s4, 64
	v_cmp_gt_i32_e64 s[12:13], s4, v129
	s_sub_i32 s4, s4, 64
	v_cmp_gt_i32_e64 s[14:15], s4, v129
	s_sub_i32 s4, s4, 64
	v_cmp_gt_i32_e32 vcc, s4, v129
	s_sub_i32 s4, s4, 64
	s_waitcnt vmcnt(16)
	v_cndmask_b32_e64 v85, 0, v85, s[10:11]
	v_cndmask_b32_e64 v84, 0, v84, s[12:13]
	v_cndmask_b32_e64 v83, 0, v83, s[14:15]
	v_cndmask_b32_e32 v82, 0, v82, vcc
	v_cmp_gt_i32_e64 s[10:11], s4, v129
	s_sub_i32 s4, s4, 64
	v_cmp_gt_i32_e64 s[12:13], s4, v129
	s_sub_i32 s4, s4, 64
	v_cmp_gt_i32_e64 s[14:15], s4, v129
	s_sub_i32 s4, s4, 64
	v_cmp_gt_i32_e32 vcc, s4, v129
	s_sub_i32 s4, s4, 64
	s_waitcnt vmcnt(12)
	v_cndmask_b32_e64 v81, 0, v81, s[10:11]
	v_cndmask_b32_e64 v80, 0, v80, s[12:13]
	v_cndmask_b32_e64 v79, 0, v79, s[14:15]
	v_cndmask_b32_e32 v78, 0, v78, vcc
	v_cmp_gt_i32_e64 s[10:11], s4, v129
	s_sub_i32 s4, s4, 64
	v_cmp_gt_i32_e64 s[12:13], s4, v129
	s_sub_i32 s4, s4, 64
	v_cmp_gt_i32_e64 s[14:15], s4, v129
	s_sub_i32 s4, s4, 64
	v_cmp_gt_i32_e32 vcc, s4, v129
	s_sub_i32 s4, s4, 64
	s_waitcnt vmcnt(8)
	v_cndmask_b32_e64 v77, 0, v77, s[10:11]
	v_cndmask_b32_e64 v76, 0, v76, s[12:13]
	v_cndmask_b32_e64 v75, 0, v75, s[14:15]
	v_cndmask_b32_e32 v74, 0, v74, vcc
	v_cmp_gt_i32_e64 s[10:11], s4, v129
	s_sub_i32 s4, s4, 64
	v_cmp_gt_i32_e64 s[12:13], s4, v129
	s_sub_i32 s4, s4, 64
	v_cmp_gt_i32_e64 s[14:15], s4, v129
	s_sub_i32 s4, s4, 64
	v_cmp_gt_i32_e32 vcc, s4, v129
	s_sub_i32 s4, s4, 64
	s_waitcnt vmcnt(4)
	v_cndmask_b32_e64 v73, 0, v73, s[10:11]
	v_cndmask_b32_e64 v72, 0, v72, s[12:13]
	v_cndmask_b32_e64 v71, 0, v71, s[14:15]
	v_cndmask_b32_e32 v70, 0, v70, vcc
	v_cmp_gt_i32_e64 s[10:11], s4, v129
	s_sub_i32 s4, s4, 64
	v_cmp_gt_i32_e64 s[12:13], s4, v129
	s_sub_i32 s4, s4, 64
	v_cmp_gt_i32_e64 s[14:15], s4, v129
	s_sub_i32 s4, s4, 64
	v_cmp_gt_i32_e32 vcc, s4, v129
	s_sub_i32 s4, s4, 64
	s_waitcnt vmcnt(0)
	v_cndmask_b32_e64 v68, 0, v68, s[10:11]
	v_cndmask_b32_e64 v66, 0, v66, s[12:13]
	v_cndmask_b32_e64 v64, 0, v64, s[14:15]
	v_cndmask_b32_e32 v57, 0, v57, vcc
	s_branch .LBB0_729

; #define LDS_WAIT() asm volatile("s_waitcnt lgkmcnt(0)" ::: "memory")
; #define SHI(v, s) bperm_((s), (v))
; __device__ __forceinline__ bool dsa2_sampled(LAS unsigned char* wl, const unsigned (&kk)[128], int nreg, int n, int lane) {
;     ...
;             const unsigned bf = (unsigned)SHI(lane * 4 + bs, src); const unsigned aa = (unsigned)SHI((int)a, src); const unsigned hb = (unsigned)SHI((int)(bs == 3 ? h4[3] : bs == 2 ? h4[2] : bs == 1 ? h4[1] : h4[0]), src);
;             prefix = (prefix << w) | bf; need -= aa; shf = sh;
;             LDS_WAIT();
;             if (hb == need) break; }
.LBB0_1251:
	s_or_b64 exec, exec, s[2:3]
	s_lshr_b32 s4, s62, 2
	s_nop 0
	v_readlane_b32 s5, v3, s4
	s_add_i32 s59, s59, 1
	v_sub_u32_e32 v8, v8, v11
	s_cmp_eq_u32 s59, 6
	s_cselect_b64 s[2:3], -1, 0
	v_mov_b32_e32 v0, s5
	v_cmp_eq_u32_e32 vcc, v0, v8
	s_waitcnt lgkmcnt(0)
	s_or_b64 s[2:3], vcc, s[2:3]
	v_lshlrev_b64 v[4:5], s61, v[4:5]
	s_and_b64 s[2:3], exec, s[2:3]
	v_or_b32_e32 v4, v4, v10
	s_or_b64 s[12:13], s[2:3], s[12:13]
	v_mov_b32_e32 v0, s60
	s_mov_b32 s62, s60
	s_andn2_b64 exec, exec, s[12:13]
	s_cbranch_execz .LBB0_1263

; #define LAS __attribute__((address_space(3)))
; #define SHI(v, s) bperm_((s), (v))
; __device__ __forceinline__ bool dsa2_sampled(LAS unsigned char* wl, const unsigned (&kk)[128], int nreg, int n, int lane) {
;     ...
;             const v4u v = *(const LAS v4u*)(h2 + 4 * lane); const unsigned m4 = (v.x + v.y) + (v.z + v.w); const unsigned pr2_ = dpp_scan_add_u32(m4); const unsigned in2 = (unsigned)__builtin_amdgcn_readlane((int)pr2_, 63) - pr2_ + m4;
;             const unsigned ab = in2 - m4; const bool fnd = ab < need && need <= ab + m4;
;             unsigned a = ab; int bs = 0; bool dn = false; const unsigned h4[4] = {v.x, v.y, v.z, v.w};
; #pragma unroll
;             for (int i = 3; i >= 0; --i) { const bool hit = !dn && (need <= a + h4[i]); bs = hit ? i : bs; a = (dn || hit) ? a : a + h4[i]; dn = dn || hit; }
;             const int src = __builtin_ctzll(__ballot(fnd));
;             const unsigned bf = (unsigned)SHI(lane * 4 + bs, src); const unsigned aa = (unsigned)SHI((int)a, src); const unsigned hb = (unsigned)SHI((int)(bs == 3 ? h4[3] : bs == 2 ? h4[2] : bs == 1 ? h4[1] : h4[0]), src);
;             prefix = (prefix << w) | bf; need -= aa; shf = sh;
.LBB0_1258:
	s_waitcnt lgkmcnt(0)
	ds_read_b128 v[0:3], v9 offset:13312
	s_waitcnt lgkmcnt(0)
	v_add_u32_e32 v10, v0, v1
	v_add3_u32 v10, v10, v3, v2
	s_nop 1
	v_add_u32_dpp v11, v10, v10 row_shr:1 row_mask:0xf bank_mask:0xf bound_ctrl:1
	s_nop 1
	v_add_u32_dpp v11, v11, v11 row_shr:2 row_mask:0xf bank_mask:0xf bound_ctrl:1
	s_nop 1
	v_add_u32_dpp v11, v11, v11 row_shr:4 row_mask:0xf bank_mask:0xf bound_ctrl:1
	s_nop 1
	v_add_u32_dpp v11, v11, v11 row_shr:8 row_mask:0xf bank_mask:0xf bound_ctrl:1
	s_nop 1
	v_add_u32_dpp v11, v11, v11 row_bcast:15 row_mask:0xa bank_mask:0xf
	s_nop 1
	v_add_u32_dpp v11, v11, v11 row_bcast:31 row_mask:0xc bank_mask:0xf
	s_nop 0
	v_readlane_b32 s2, v11, 63
	s_nop 1
	v_sub_u32_e32 v11, s2, v11
	v_add_u32_e32 v12, v11, v3
	v_add_u32_e32 v10, v11, v10
	v_cmp_le_u32_e64 s[2:3], v8, v12
	v_cmp_le_u32_e32 vcc, v8, v10
	s_nop 0
	v_cndmask_b32_e64 v10, v3, 0, s[2:3]
	v_add_u32_e32 v10, v10, v11
	v_add_u32_e32 v12, v10, v2
	v_cmp_le_u32_e64 s[4:5], v8, v12
	s_nop 1
	v_cndmask_b32_e64 v12, 0, 2, s[4:5]
	v_cndmask_b32_e64 v12, v12, 3, s[2:3]
	s_or_b64 s[2:3], s[2:3], s[4:5]
	v_cndmask_b32_e64 v13, v2, 0, s[2:3]
	v_add_u32_e32 v10, v13, v10
	v_add_u32_e32 v13, v10, v1
	v_cmp_le_u32_e64 s[4:5], v8, v13
	s_nop 1
	v_cndmask_b32_e64 v13, v12, 1, s[4:5]
	v_cndmask_b32_e64 v12, v13, v12, s[2:3]
	s_or_b64 s[2:3], s[2:3], s[4:5]
	v_cndmask_b32_e64 v13, v1, 0, s[2:3]
	v_add_u32_e32 v10, v13, v10
	v_add_u32_e32 v13, v10, v0
	v_cmp_le_u32_e64 s[4:5], v8, v13
	s_nop 1
	v_cndmask_b32_e64 v13, v12, 0, s[4:5]
	v_cndmask_b32_e64 v12, v13, v12, s[2:3]
	s_or_b64 s[2:3], s[2:3], s[4:5]
	v_cndmask_b32_e64 v13, v0, 0, s[2:3]
	v_cmp_lt_u32_e64 s[2:3], v11, v8
	s_and_b64 s[2:3], s[2:3], vcc
	v_add_u32_e32 v13, v13, v10
	v_cndmask_b32_e64 v10, 0, 1, s[2:3]
	v_cmp_ne_u32_e32 vcc, 0, v10
	s_ff1_i32_b64 s2, vcc
	s_lshl_b32 s62, s2, 2
	v_or_b32_e32 v10, v12, v7
	s_nop 0
	v_readlane_b32 s4, v10, s2
	v_readlane_b32 s5, v13, s2
	s_nop 0
	v_mov_b32_e32 v10, s4
	v_mov_b32_e32 v11, s5
	v_cmp_gt_i32_e32 vcc, 3, v12
	s_and_saveexec_b64 s[2:3], vcc
	s_cbranch_execz .LBB0_1251
	v_cmp_ne_u32_e32 vcc, 2, v12
	s_and_saveexec_b64 s[4:5], vcc
	s_xor_b64 s[4:5], exec, s[4:5]
	v_cmp_eq_u32_e32 vcc, 1, v12
	s_nop 1
	v_cndmask_b32_e32 v3, v0, v1, vcc
	s_andn2_saveexec_b64 s[4:5], s[4:5]
	s_cbranch_execz .LBB0_1250
	v_mov_b32_e32 v3, v2
	s_branch .LBB0_1250
